# expert GEMM 1 epilogue: SwiGLU element chains issued pairwise interleaved on two scratch registers (no one-state pads behind exp/rcp)
# baseline (speedup 1.0000x reference)
.LBB0_1265:
	v_mov_b32_e32 v8, v0
	v_ashrrev_i32_e32 v181, 31, v180
	v_ashrrev_i32_e32 v2, 2, v8
	v_and_b32_e32 v6, 0xffffffc0, v2
	v_lshlrev_b64 v[4:5], 8, v[180:181]
	v_ashrrev_i32_e32 v7, 31, v6
	v_and_or_b32 v6, v8, 15, v6
	v_bfe_u32 v12, v8, 4, 1
	v_lshl_add_u64 v[10:11], v[6:7], 0, v[4:5]
	v_lshlrev_b32_e32 v4, 3, v12
	v_lshrrev_b32_e32 v2, 1, v8
	v_sub_co_u32_e32 v8, vcc, 0, v4
	v_min_f32_e32 v4, 0x40e00000, v176
	s_nop 0
	v_subb_co_u32_e64 v9, s[2:3], 0, 0, vcc
	s_mov_b32 s2, 0xc1c00000
	v_med3_f32 v5, v172, s2, v200
	v_mul_f32_e32 v5, v4, v5
	v_mul_f32_e32 v4, 0xc01d265f, v4
	v_exp_f32_e32 v4, v4
	v_med3_f32 v6, v173, s2, v200
	v_med3_f32 v7, v174, s2, v200
	v_med3_f32 v13, v175, s2, v200
	v_add_f32_e32 v4, 1.0, v4
	v_rcp_f32_e32 v4, v4
	v_med3_f32 v14, v164, s2, v200
	v_med3_f32 v15, v165, s2, v200
	v_med3_f32 v16, v166, s2, v200
	v_mul_f32_e32 v5, v4, v5
	v_med3_f32 v17, v167, s2, v200
	v_med3_f32 v18, v150, s2, v200
	v_med3_f32 v19, v151, s2, v200
	v_lshlrev_b32_e32 v12, 4, v12
	s_lshl_b32 s12, s26, 7
	s_ashr_i32 s13, s12, 31
	v_and_b32_e32 v2, 0x78, v2
	v_med3_f32 v20, v87, s2, v200
	s_and_b64 vcc, exec, s[40:41]
	v_min_f32_e32 v4, 0x40e00000, v177
	v_min_f32_e32 v194, 0x40e00000, v178
	v_mul_f32_e32 v6, v4, v6
	v_mul_f32_e32 v7, v194, v7
	v_mul_f32_e32 v4, 0xc01d265f, v4
	v_mul_f32_e32 v194, 0xc01d265f, v194
	v_exp_f32_e32 v4, v4
	v_exp_f32_e32 v194, v194
	v_add_f32_e32 v4, 1.0, v4
	v_add_f32_e32 v194, 1.0, v194
	v_rcp_f32_e32 v4, v4
	v_rcp_f32_e32 v194, v194
	v_mul_f32_e32 v6, v4, v6
	v_mul_f32_e32 v7, v194, v7
	v_min_f32_e32 v4, 0x40e00000, v179
	v_min_f32_e32 v194, 0x40e00000, v168
	v_mul_f32_e32 v13, v4, v13
	v_mul_f32_e32 v14, v194, v14
	v_mul_f32_e32 v4, 0xc01d265f, v4
	v_mul_f32_e32 v194, 0xc01d265f, v194
	v_exp_f32_e32 v4, v4
	v_exp_f32_e32 v194, v194
	v_add_f32_e32 v4, 1.0, v4
	v_add_f32_e32 v194, 1.0, v194
	v_rcp_f32_e32 v4, v4
	v_rcp_f32_e32 v194, v194
	v_mul_f32_e32 v13, v4, v13
	v_mul_f32_e32 v14, v194, v14
	v_min_f32_e32 v4, 0x40e00000, v169
	v_min_f32_e32 v194, 0x40e00000, v170
	v_mul_f32_e32 v15, v4, v15
	v_mul_f32_e32 v16, v194, v16
	v_mul_f32_e32 v4, 0xc01d265f, v4
	v_mul_f32_e32 v194, 0xc01d265f, v194
	v_exp_f32_e32 v4, v4
	v_exp_f32_e32 v194, v194
	v_add_f32_e32 v4, 1.0, v4
	v_add_f32_e32 v194, 1.0, v194
	v_rcp_f32_e32 v4, v4
	v_rcp_f32_e32 v194, v194
	v_mul_f32_e32 v15, v4, v15
	v_mul_f32_e32 v16, v194, v16
	v_min_f32_e32 v4, 0x40e00000, v171
	v_mul_f32_e32 v17, v4, v17
	v_mul_f32_e32 v4, 0xc01d265f, v4
	v_exp_f32_e32 v4, v4
	s_nop 0
	v_add_f32_e32 v4, 1.0, v4
	v_rcp_f32_e32 v4, v4
	s_nop 0
	v_mul_f32_e32 v17, v4, v17
	v_mov_b32_e32 v4, v3
	v_cvt_pk_fp8_f32 v4, v5, v6
	v_min_f32_e32 v6, 0x40e00000, v160
	v_mov_b32_e32 v5, v3
	v_cvt_pk_fp8_f32 v4, v7, v13 op_sel:[0,0,1]
	v_med3_f32 v7, v156, s2, v200
	v_mul_f32_e32 v7, v6, v7
	v_mul_f32_e32 v6, 0xc01d265f, v6
	v_exp_f32_e32 v6, v6
	v_med3_f32 v13, v157, s2, v200
	v_cvt_pk_fp8_f32 v5, v14, v15
	v_med3_f32 v14, v158, s2, v200
	v_add_f32_e32 v6, 1.0, v6
	v_rcp_f32_e32 v6, v6
	v_med3_f32 v15, v159, s2, v200
	v_cvt_pk_fp8_f32 v5, v16, v17 op_sel:[0,0,1]
	v_med3_f32 v16, v148, s2, v200
	v_mul_f32_e32 v7, v6, v7
	v_med3_f32 v17, v149, s2, v200
	v_min_f32_e32 v6, 0x40e00000, v161
	v_min_f32_e32 v194, 0x40e00000, v162
	v_mul_f32_e32 v13, v6, v13
	v_mul_f32_e32 v14, v194, v14
	v_mul_f32_e32 v6, 0xc01d265f, v6
	v_mul_f32_e32 v194, 0xc01d265f, v194
	v_exp_f32_e32 v6, v6
	v_exp_f32_e32 v194, v194
	v_add_f32_e32 v6, 1.0, v6
	v_add_f32_e32 v194, 1.0, v194
	v_rcp_f32_e32 v6, v6
	v_rcp_f32_e32 v194, v194
	v_mul_f32_e32 v13, v6, v13
	v_mul_f32_e32 v14, v194, v14
	v_min_f32_e32 v6, 0x40e00000, v163
	v_min_f32_e32 v194, 0x40e00000, v152
	v_mul_f32_e32 v15, v6, v15
	v_mul_f32_e32 v16, v194, v16
	v_mul_f32_e32 v6, 0xc01d265f, v6
	v_mul_f32_e32 v194, 0xc01d265f, v194
	v_exp_f32_e32 v6, v6
	v_exp_f32_e32 v194, v194
	v_add_f32_e32 v6, 1.0, v6
	v_add_f32_e32 v194, 1.0, v194
	v_rcp_f32_e32 v6, v6
	v_rcp_f32_e32 v194, v194
	v_mul_f32_e32 v15, v6, v15
	v_mul_f32_e32 v16, v194, v16
	v_min_f32_e32 v6, 0x40e00000, v153
	v_min_f32_e32 v194, 0x40e00000, v154
	v_mul_f32_e32 v17, v6, v17
	v_mul_f32_e32 v18, v194, v18
	v_mul_f32_e32 v6, 0xc01d265f, v6
	v_mul_f32_e32 v194, 0xc01d265f, v194
	v_exp_f32_e32 v6, v6
	v_exp_f32_e32 v194, v194
	v_add_f32_e32 v6, 1.0, v6
	v_add_f32_e32 v194, 1.0, v194
	v_rcp_f32_e32 v6, v6
	v_rcp_f32_e32 v194, v194
	v_mul_f32_e32 v17, v6, v17
	v_mul_f32_e32 v18, v194, v18
	v_min_f32_e32 v6, 0x40e00000, v155
	v_mul_f32_e32 v19, v6, v19
	v_mul_f32_e32 v6, 0xc01d265f, v6
	v_exp_f32_e32 v6, v6
	s_nop 0
	v_add_f32_e32 v6, 1.0, v6
	v_rcp_f32_e32 v6, v6
	s_nop 0
	v_mul_f32_e32 v19, v6, v19
	v_mov_b32_e32 v6, v3
	v_cvt_pk_fp8_f32 v6, v7, v13
	v_mov_b32_e32 v7, v3
	v_cvt_pk_fp8_f32 v7, v16, v17
	v_med3_f32 v13, v143, s2, v200
	v_cvt_pk_fp8_f32 v6, v14, v15 op_sel:[0,0,1]
	v_or_b32_e32 v14, v10, v12
	v_mov_b32_e32 v15, v11
	v_cvt_pk_fp8_f32 v7, v18, v19 op_sel:[0,0,1]
	v_lshlrev_b64 v[14:15], 10, v[14:15]
	v_lshl_add_u64 v[14:15], s[10:11], 0, v[14:15]
	v_lshl_add_u64 v[14:15], v[14:15], 0, s[12:13]
	v_lshl_add_u64 v[14:15], v[14:15], 0, v[2:3]
	v_permlane16_swap_b32_e32 v4, v6
	v_permlane16_swap_b32_e32 v5, v7
	v_lshl_add_u64 v[14:15], v[14:15], 0, v[8:9]
	global_store_dwordx4 v[14:15], v[4:7], off
	v_med3_f32 v14, v132, s2, v200
	v_med3_f32 v15, v133, s2, v200
	v_min_f32_e32 v4, 0x40e00000, v144
	v_med3_f32 v5, v140, s2, v200
	v_mul_f32_e32 v5, v4, v5
	v_mul_f32_e32 v4, 0xc01d265f, v4
	v_exp_f32_e32 v4, v4
	v_med3_f32 v6, v141, s2, v200
	v_med3_f32 v7, v142, s2, v200
	v_med3_f32 v16, v134, s2, v200
	v_add_f32_e32 v4, 1.0, v4
	v_rcp_f32_e32 v4, v4
	v_med3_f32 v17, v135, s2, v200
	v_med3_f32 v18, v118, s2, v200
	v_med3_f32 v19, v119, s2, v200
	v_mul_f32_e32 v5, v4, v5
	v_min_f32_e32 v4, 0x40e00000, v145
	v_min_f32_e32 v194, 0x40e00000, v146
	v_mul_f32_e32 v6, v4, v6
	v_mul_f32_e32 v7, v194, v7
	v_mul_f32_e32 v4, 0xc01d265f, v4
	v_mul_f32_e32 v194, 0xc01d265f, v194
	v_exp_f32_e32 v4, v4
	v_exp_f32_e32 v194, v194
	v_add_f32_e32 v4, 1.0, v4
	v_add_f32_e32 v194, 1.0, v194
	v_rcp_f32_e32 v4, v4
	v_rcp_f32_e32 v194, v194
	v_mul_f32_e32 v6, v4, v6
	v_mul_f32_e32 v7, v194, v7
	v_min_f32_e32 v4, 0x40e00000, v147
	v_min_f32_e32 v194, 0x40e00000, v136
	v_mul_f32_e32 v13, v4, v13
	v_mul_f32_e32 v14, v194, v14
	v_mul_f32_e32 v4, 0xc01d265f, v4
	v_mul_f32_e32 v194, 0xc01d265f, v194
	v_exp_f32_e32 v4, v4
	v_exp_f32_e32 v194, v194
	v_add_f32_e32 v4, 1.0, v4
	v_add_f32_e32 v194, 1.0, v194
	v_rcp_f32_e32 v4, v4
	v_rcp_f32_e32 v194, v194
	v_mul_f32_e32 v13, v4, v13
	v_mul_f32_e32 v14, v194, v14
	v_min_f32_e32 v4, 0x40e00000, v137
	v_min_f32_e32 v194, 0x40e00000, v138
	v_mul_f32_e32 v15, v4, v15
	v_mul_f32_e32 v16, v194, v16
	v_mul_f32_e32 v4, 0xc01d265f, v4
	v_mul_f32_e32 v194, 0xc01d265f, v194
	v_exp_f32_e32 v4, v4
	v_exp_f32_e32 v194, v194
	v_add_f32_e32 v4, 1.0, v4
	v_add_f32_e32 v194, 1.0, v194
	v_rcp_f32_e32 v4, v4
	v_rcp_f32_e32 v194, v194
	v_mul_f32_e32 v15, v4, v15
	v_mul_f32_e32 v16, v194, v16
	v_min_f32_e32 v4, 0x40e00000, v139
	v_mul_f32_e32 v17, v4, v17
	v_mul_f32_e32 v4, 0xc01d265f, v4
	v_exp_f32_e32 v4, v4
	s_nop 0
	v_add_f32_e32 v4, 1.0, v4
	v_rcp_f32_e32 v4, v4
	s_nop 0
	v_mul_f32_e32 v17, v4, v17
	v_mov_b32_e32 v4, v3
	v_cvt_pk_fp8_f32 v4, v5, v6
	v_min_f32_e32 v6, 0x40e00000, v128
	v_mov_b32_e32 v5, v3
	v_cvt_pk_fp8_f32 v4, v7, v13 op_sel:[0,0,1]
	v_med3_f32 v7, v124, s2, v200
	v_mul_f32_e32 v7, v6, v7
	v_mul_f32_e32 v6, 0xc01d265f, v6
	v_exp_f32_e32 v6, v6
	v_med3_f32 v13, v125, s2, v200
	v_cvt_pk_fp8_f32 v5, v14, v15
	v_med3_f32 v14, v126, s2, v200
	v_add_f32_e32 v6, 1.0, v6
	v_rcp_f32_e32 v6, v6
	v_med3_f32 v15, v127, s2, v200
	v_cvt_pk_fp8_f32 v5, v16, v17 op_sel:[0,0,1]
	v_med3_f32 v16, v116, s2, v200
	v_mul_f32_e32 v7, v6, v7
	v_med3_f32 v17, v117, s2, v200
	v_min_f32_e32 v6, 0x40e00000, v129
	v_min_f32_e32 v194, 0x40e00000, v130
	v_mul_f32_e32 v13, v6, v13
	v_mul_f32_e32 v14, v194, v14
	v_mul_f32_e32 v6, 0xc01d265f, v6
	v_mul_f32_e32 v194, 0xc01d265f, v194
	v_exp_f32_e32 v6, v6
	v_exp_f32_e32 v194, v194
	v_add_f32_e32 v6, 1.0, v6
	v_add_f32_e32 v194, 1.0, v194
	v_rcp_f32_e32 v6, v6
	v_rcp_f32_e32 v194, v194
	v_mul_f32_e32 v13, v6, v13
	v_mul_f32_e32 v14, v194, v14
	v_min_f32_e32 v6, 0x40e00000, v131
	v_min_f32_e32 v194, 0x40e00000, v120
	v_mul_f32_e32 v15, v6, v15
	v_mul_f32_e32 v16, v194, v16
	v_mul_f32_e32 v6, 0xc01d265f, v6
	v_mul_f32_e32 v194, 0xc01d265f, v194
	v_exp_f32_e32 v6, v6
	v_exp_f32_e32 v194, v194
	v_add_f32_e32 v6, 1.0, v6
	v_add_f32_e32 v194, 1.0, v194
	v_rcp_f32_e32 v6, v6
	v_rcp_f32_e32 v194, v194
	v_mul_f32_e32 v15, v6, v15
	v_mul_f32_e32 v16, v194, v16
	v_min_f32_e32 v6, 0x40e00000, v121
	v_min_f32_e32 v194, 0x40e00000, v122
	v_mul_f32_e32 v17, v6, v17
	v_mul_f32_e32 v18, v194, v18
	v_mul_f32_e32 v6, 0xc01d265f, v6
	v_mul_f32_e32 v194, 0xc01d265f, v194
	v_exp_f32_e32 v6, v6
	v_exp_f32_e32 v194, v194
	v_add_f32_e32 v6, 1.0, v6
	v_add_f32_e32 v194, 1.0, v194
	v_rcp_f32_e32 v6, v6
	v_rcp_f32_e32 v194, v194
	v_mul_f32_e32 v17, v6, v17
	v_mul_f32_e32 v18, v194, v18
	v_min_f32_e32 v6, 0x40e00000, v123
	v_mul_f32_e32 v19, v6, v19
	v_mul_f32_e32 v6, 0xc01d265f, v6
	v_exp_f32_e32 v6, v6
	s_nop 0
	v_add_f32_e32 v6, 1.0, v6
	v_rcp_f32_e32 v6, v6
	s_nop 0
	v_mul_f32_e32 v19, v6, v19
	v_mov_b32_e32 v6, v3
	v_cvt_pk_fp8_f32 v6, v7, v13
	v_mov_b32_e32 v7, v3
	v_cvt_pk_fp8_f32 v7, v16, v17
	v_or_b32_e32 v13, 32, v12
	v_cvt_pk_fp8_f32 v6, v14, v15 op_sel:[0,0,1]
	v_or_b32_e32 v14, v10, v13
	v_mov_b32_e32 v15, v11
	v_cvt_pk_fp8_f32 v7, v18, v19 op_sel:[0,0,1]
	v_lshlrev_b64 v[14:15], 10, v[14:15]
	v_lshl_add_u64 v[14:15], s[10:11], 0, v[14:15]
	v_lshl_add_u64 v[14:15], v[14:15], 0, s[12:13]
	v_lshl_add_u64 v[14:15], v[14:15], 0, v[2:3]
	v_permlane16_swap_b32_e32 v4, v6
	v_permlane16_swap_b32_e32 v5, v7
	v_lshl_add_u64 v[14:15], v[14:15], 0, v[8:9]
	global_store_dwordx4 v[14:15], v[4:7], off
	v_med3_f32 v14, v111, s2, v200
	v_med3_f32 v15, v100, s2, v200
	v_min_f32_e32 v4, 0x40e00000, v112
	v_med3_f32 v5, v108, s2, v200
	v_mul_f32_e32 v5, v4, v5
	v_mul_f32_e32 v4, 0xc01d265f, v4
	v_exp_f32_e32 v4, v4
	v_med3_f32 v6, v109, s2, v200
	v_med3_f32 v7, v110, s2, v200
	v_med3_f32 v16, v101, s2, v200
	v_add_f32_e32 v4, 1.0, v4
	v_rcp_f32_e32 v4, v4
	v_med3_f32 v17, v102, s2, v200
	v_med3_f32 v18, v103, s2, v200
	v_med3_f32 v19, v86, s2, v200
	v_mul_f32_e32 v5, v4, v5
	v_lshl_add_u64 v[10:11], v[10:11], 0, s[52:53]
	v_min_f32_e32 v4, 0x40e00000, v113
	v_min_f32_e32 v194, 0x40e00000, v114
	v_mul_f32_e32 v6, v4, v6
	v_mul_f32_e32 v7, v194, v7
	v_mul_f32_e32 v4, 0xc01d265f, v4
	v_mul_f32_e32 v194, 0xc01d265f, v194
	v_exp_f32_e32 v4, v4
	v_exp_f32_e32 v194, v194
	v_add_f32_e32 v4, 1.0, v4
	v_add_f32_e32 v194, 1.0, v194
	v_rcp_f32_e32 v4, v4
	v_rcp_f32_e32 v194, v194
	v_mul_f32_e32 v6, v4, v6
	v_mul_f32_e32 v7, v194, v7
	v_min_f32_e32 v4, 0x40e00000, v115
	v_min_f32_e32 v194, 0x40e00000, v104
	v_mul_f32_e32 v14, v4, v14
	v_mul_f32_e32 v15, v194, v15
	v_mul_f32_e32 v4, 0xc01d265f, v4
	v_mul_f32_e32 v194, 0xc01d265f, v194
	v_exp_f32_e32 v4, v4
	v_exp_f32_e32 v194, v194
	v_add_f32_e32 v4, 1.0, v4
	v_add_f32_e32 v194, 1.0, v194
	v_rcp_f32_e32 v4, v4
	v_rcp_f32_e32 v194, v194
	v_mul_f32_e32 v14, v4, v14
	v_mul_f32_e32 v15, v194, v15
	v_min_f32_e32 v4, 0x40e00000, v105
	v_min_f32_e32 v194, 0x40e00000, v106
	v_mul_f32_e32 v16, v4, v16
	v_mul_f32_e32 v17, v194, v17
	v_mul_f32_e32 v4, 0xc01d265f, v4
	v_mul_f32_e32 v194, 0xc01d265f, v194
	v_exp_f32_e32 v4, v4
	v_exp_f32_e32 v194, v194
	v_add_f32_e32 v4, 1.0, v4
	v_add_f32_e32 v194, 1.0, v194
	v_rcp_f32_e32 v4, v4
	v_rcp_f32_e32 v194, v194
	v_mul_f32_e32 v16, v4, v16
	v_mul_f32_e32 v17, v194, v17
	v_min_f32_e32 v4, 0x40e00000, v107
	v_mul_f32_e32 v18, v4, v18
	v_mul_f32_e32 v4, 0xc01d265f, v4
	v_exp_f32_e32 v4, v4
	s_nop 0
	v_add_f32_e32 v4, 1.0, v4
	v_rcp_f32_e32 v4, v4
	s_nop 0
	v_mul_f32_e32 v18, v4, v18
	v_mov_b32_e32 v4, v3
	v_cvt_pk_fp8_f32 v4, v5, v6
	v_min_f32_e32 v6, 0x40e00000, v96
	v_mov_b32_e32 v5, v3
	v_cvt_pk_fp8_f32 v4, v7, v14 op_sel:[0,0,1]
	v_med3_f32 v7, v92, s2, v200
	v_mul_f32_e32 v7, v6, v7
	v_mul_f32_e32 v6, 0xc01d265f, v6
	v_exp_f32_e32 v6, v6
	v_med3_f32 v14, v93, s2, v200
	v_cvt_pk_fp8_f32 v5, v15, v16
	v_med3_f32 v15, v94, s2, v200
	v_add_f32_e32 v6, 1.0, v6
	v_rcp_f32_e32 v6, v6
	v_med3_f32 v16, v95, s2, v200
	v_cvt_pk_fp8_f32 v5, v17, v18 op_sel:[0,0,1]
	v_med3_f32 v17, v84, s2, v200
	v_mul_f32_e32 v7, v6, v7
	v_med3_f32 v18, v85, s2, v200
	v_min_f32_e32 v6, 0x40e00000, v97
	v_min_f32_e32 v194, 0x40e00000, v98
	v_mul_f32_e32 v14, v6, v14
	v_mul_f32_e32 v15, v194, v15
	v_mul_f32_e32 v6, 0xc01d265f, v6
	v_mul_f32_e32 v194, 0xc01d265f, v194
	v_exp_f32_e32 v6, v6
	v_exp_f32_e32 v194, v194
	v_add_f32_e32 v6, 1.0, v6
	v_add_f32_e32 v194, 1.0, v194
	v_rcp_f32_e32 v6, v6
	v_rcp_f32_e32 v194, v194
	v_mul_f32_e32 v14, v6, v14
	v_mul_f32_e32 v15, v194, v15
	v_min_f32_e32 v6, 0x40e00000, v99
	v_min_f32_e32 v194, 0x40e00000, v88
	v_mul_f32_e32 v16, v6, v16
	v_mul_f32_e32 v17, v194, v17
	v_mul_f32_e32 v6, 0xc01d265f, v6
	v_mul_f32_e32 v194, 0xc01d265f, v194
	v_exp_f32_e32 v6, v6
	v_exp_f32_e32 v194, v194
	v_add_f32_e32 v6, 1.0, v6
	v_add_f32_e32 v194, 1.0, v194
	v_rcp_f32_e32 v6, v6
	v_rcp_f32_e32 v194, v194
	v_mul_f32_e32 v16, v6, v16
	v_mul_f32_e32 v17, v194, v17
	v_min_f32_e32 v6, 0x40e00000, v89
	v_min_f32_e32 v194, 0x40e00000, v90
	v_mul_f32_e32 v18, v6, v18
	v_mul_f32_e32 v19, v194, v19
	v_mul_f32_e32 v6, 0xc01d265f, v6
	v_mul_f32_e32 v194, 0xc01d265f, v194
	v_exp_f32_e32 v6, v6
	v_exp_f32_e32 v194, v194
	v_add_f32_e32 v6, 1.0, v6
	v_add_f32_e32 v194, 1.0, v194
	v_rcp_f32_e32 v6, v6
	v_rcp_f32_e32 v194, v194
	v_mul_f32_e32 v18, v6, v18
	v_mul_f32_e32 v19, v194, v19
	v_min_f32_e32 v6, 0x40e00000, v91
	v_mul_f32_e32 v20, v6, v20
	v_mul_f32_e32 v6, 0xc01d265f, v6
	v_exp_f32_e32 v6, v6
	s_nop 0
	v_add_f32_e32 v6, 1.0, v6
	v_rcp_f32_e32 v6, v6
	s_nop 0
	v_mul_f32_e32 v20, v6, v20
	v_mov_b32_e32 v6, v3
	v_cvt_pk_fp8_f32 v6, v7, v14
	v_mov_b32_e32 v7, v3
	v_cvt_pk_fp8_f32 v7, v17, v18
	v_or_b32_e32 v14, v10, v12
	v_cvt_pk_fp8_f32 v6, v15, v16 op_sel:[0,0,1]
	v_mov_b32_e32 v15, v11
	v_cvt_pk_fp8_f32 v7, v19, v20 op_sel:[0,0,1]
	v_lshlrev_b64 v[14:15], 10, v[14:15]
	v_lshl_add_u64 v[14:15], s[10:11], 0, v[14:15]
	v_lshl_add_u64 v[14:15], v[14:15], 0, s[12:13]
	v_lshl_add_u64 v[14:15], v[14:15], 0, v[2:3]
	v_permlane16_swap_b32_e32 v4, v6
	v_permlane16_swap_b32_e32 v5, v7
	v_lshl_add_u64 v[14:15], v[14:15], 0, v[8:9]
	global_store_dwordx4 v[14:15], v[4:7], off
	v_med3_f32 v12, v79, s2, v200
	v_med3_f32 v14, v68, s2, v200
	v_min_f32_e32 v4, 0x40e00000, v80
	v_med3_f32 v5, v76, s2, v200
	v_mul_f32_e32 v5, v4, v5
	v_mul_f32_e32 v4, 0xc01d265f, v4
	v_exp_f32_e32 v4, v4
	v_med3_f32 v6, v77, s2, v200
	v_med3_f32 v7, v78, s2, v200
	v_med3_f32 v15, v69, s2, v200
	v_add_f32_e32 v4, 1.0, v4
	v_rcp_f32_e32 v4, v4
	v_med3_f32 v16, v70, s2, v200
	v_med3_f32 v17, v71, s2, v200
	v_med3_f32 v18, v54, s2, v200
	v_mul_f32_e32 v5, v4, v5
	v_med3_f32 v19, v55, s2, v200
	v_or_b32_e32 v10, v10, v13
	v_lshlrev_b64 v[10:11], 10, v[10:11]
	v_lshl_add_u64 v[10:11], s[10:11], 0, v[10:11]
	v_lshl_add_u64 v[10:11], v[10:11], 0, s[12:13]
	v_lshl_add_u64 v[10:11], v[10:11], 0, v[2:3]
	v_lshl_add_u64 v[8:9], v[10:11], 0, v[8:9]
	v_min_f32_e32 v4, 0x40e00000, v81
	v_min_f32_e32 v194, 0x40e00000, v82
	v_mul_f32_e32 v6, v4, v6
	v_mul_f32_e32 v7, v194, v7
	v_mul_f32_e32 v4, 0xc01d265f, v4
	v_mul_f32_e32 v194, 0xc01d265f, v194
	v_exp_f32_e32 v4, v4
	v_exp_f32_e32 v194, v194
	v_add_f32_e32 v4, 1.0, v4
	v_add_f32_e32 v194, 1.0, v194
	v_rcp_f32_e32 v4, v4
	v_rcp_f32_e32 v194, v194
	v_mul_f32_e32 v6, v4, v6
	v_mul_f32_e32 v7, v194, v7
	v_min_f32_e32 v4, 0x40e00000, v83
	v_min_f32_e32 v194, 0x40e00000, v72
	v_mul_f32_e32 v12, v4, v12
	v_mul_f32_e32 v14, v194, v14
	v_mul_f32_e32 v4, 0xc01d265f, v4
	v_mul_f32_e32 v194, 0xc01d265f, v194
	v_exp_f32_e32 v4, v4
	v_exp_f32_e32 v194, v194
	v_add_f32_e32 v4, 1.0, v4
	v_add_f32_e32 v194, 1.0, v194
	v_rcp_f32_e32 v4, v4
	v_rcp_f32_e32 v194, v194
	v_mul_f32_e32 v12, v4, v12
	v_mul_f32_e32 v14, v194, v14
	v_min_f32_e32 v4, 0x40e00000, v73
	v_min_f32_e32 v194, 0x40e00000, v74
	v_mul_f32_e32 v15, v4, v15
	v_mul_f32_e32 v16, v194, v16
	v_mul_f32_e32 v4, 0xc01d265f, v4
	v_mul_f32_e32 v194, 0xc01d265f, v194
	v_exp_f32_e32 v4, v4
	v_exp_f32_e32 v194, v194
	v_add_f32_e32 v4, 1.0, v4
	v_add_f32_e32 v194, 1.0, v194
	v_rcp_f32_e32 v4, v4
	v_rcp_f32_e32 v194, v194
	v_mul_f32_e32 v15, v4, v15
	v_mul_f32_e32 v16, v194, v16
	v_min_f32_e32 v4, 0x40e00000, v75
	v_mul_f32_e32 v17, v4, v17
	v_mul_f32_e32 v4, 0xc01d265f, v4
	v_exp_f32_e32 v4, v4
	s_nop 0
	v_add_f32_e32 v4, 1.0, v4
	v_rcp_f32_e32 v4, v4
	s_nop 0
	v_mul_f32_e32 v17, v4, v17
	v_mov_b32_e32 v4, v3
	v_cvt_pk_fp8_f32 v4, v5, v6
	v_min_f32_e32 v6, 0x40e00000, v64
	v_mov_b32_e32 v5, v3
	v_cvt_pk_fp8_f32 v4, v7, v12 op_sel:[0,0,1]
	v_med3_f32 v7, v60, s2, v200
	v_mul_f32_e32 v7, v6, v7
	v_mul_f32_e32 v6, 0xc01d265f, v6
	v_exp_f32_e32 v6, v6
	v_med3_f32 v12, v61, s2, v200
	v_cvt_pk_fp8_f32 v5, v14, v15
	v_med3_f32 v14, v62, s2, v200
	v_add_f32_e32 v6, 1.0, v6
	v_rcp_f32_e32 v6, v6
	v_med3_f32 v15, v63, s2, v200
	v_cvt_pk_fp8_f32 v5, v16, v17 op_sel:[0,0,1]
	v_med3_f32 v16, v52, s2, v200
	v_mul_f32_e32 v7, v6, v7
	v_med3_f32 v17, v53, s2, v200
	s_mov_b64 s[2:3], -1
	v_min_f32_e32 v6, 0x40e00000, v65
	v_min_f32_e32 v194, 0x40e00000, v66
	v_mul_f32_e32 v12, v6, v12
	v_mul_f32_e32 v14, v194, v14
	v_mul_f32_e32 v6, 0xc01d265f, v6
	v_mul_f32_e32 v194, 0xc01d265f, v194
	v_exp_f32_e32 v6, v6
	v_exp_f32_e32 v194, v194
	v_add_f32_e32 v6, 1.0, v6
	v_add_f32_e32 v194, 1.0, v194
	v_rcp_f32_e32 v6, v6
	v_rcp_f32_e32 v194, v194
	v_mul_f32_e32 v12, v6, v12
	v_mul_f32_e32 v14, v194, v14
	v_min_f32_e32 v6, 0x40e00000, v67
	v_min_f32_e32 v194, 0x40e00000, v56
	v_mul_f32_e32 v15, v6, v15
	v_mul_f32_e32 v16, v194, v16
	v_mul_f32_e32 v6, 0xc01d265f, v6
	v_mul_f32_e32 v194, 0xc01d265f, v194
	v_exp_f32_e32 v6, v6
	v_exp_f32_e32 v194, v194
	v_add_f32_e32 v6, 1.0, v6
	v_add_f32_e32 v194, 1.0, v194
	v_rcp_f32_e32 v6, v6
	v_rcp_f32_e32 v194, v194
	v_mul_f32_e32 v15, v6, v15
	v_mul_f32_e32 v16, v194, v16
	v_min_f32_e32 v6, 0x40e00000, v57
	v_min_f32_e32 v194, 0x40e00000, v58
	v_mul_f32_e32 v17, v6, v17
	v_mul_f32_e32 v18, v194, v18
	v_mul_f32_e32 v6, 0xc01d265f, v6
	v_mul_f32_e32 v194, 0xc01d265f, v194
	v_exp_f32_e32 v6, v6
	v_exp_f32_e32 v194, v194
	v_add_f32_e32 v6, 1.0, v6
	v_add_f32_e32 v194, 1.0, v194
	v_rcp_f32_e32 v6, v6
	v_rcp_f32_e32 v194, v194
	v_mul_f32_e32 v17, v6, v17
	v_mul_f32_e32 v18, v194, v18
	v_min_f32_e32 v6, 0x40e00000, v59
	v_mul_f32_e32 v19, v6, v19
	v_mul_f32_e32 v6, 0xc01d265f, v6
	v_exp_f32_e32 v6, v6
	s_nop 0
	v_add_f32_e32 v6, 1.0, v6
	v_rcp_f32_e32 v6, v6
	s_nop 0
	v_mul_f32_e32 v19, v6, v19
	v_mov_b32_e32 v6, v3
	v_cvt_pk_fp8_f32 v6, v7, v12
	v_mov_b32_e32 v7, v3
	v_cvt_pk_fp8_f32 v7, v16, v17
	v_cvt_pk_fp8_f32 v6, v14, v15 op_sel:[0,0,1]
	v_cvt_pk_fp8_f32 v7, v18, v19 op_sel:[0,0,1]
	s_nop 0
	v_permlane16_swap_b32_e32 v4, v6
	v_permlane16_swap_b32_e32 v5, v7
	global_store_dwordx4 v[8:9], v[4:7], off
	s_cbranch_vccnz .LBB0_1269
	s_and_saveexec_b64 s[2:3], s[36:37]
	s_xor_b64 s[2:3], exec, s[2:3]
	s_cbranch_execz .LBB0_1268
	s_barrier
